# same K-loop edits extended to the residual-GEMM K-loop (saddr LDS-DMA, invariant B base)
# baseline (speedup 1.0000x reference)
; #define PG8_STAGE(bufoff, gbase, voff) do { _Pragma("unroll") for (int _i = 0; _i < 2; ++_i) \
;         __builtin_amdgcn_global_load_lds((const unsigned*)((const char*)(gbase) + (voff)[_i]), (PG8_LAS unsigned*)(lds + (bufoff) + ldsw + _i * 8192), 16, 0, 0); } while (0)
; #define PG8_LDA(dst, b, h) do { _Pragma("unroll") for (int m = 0; m < 4; ++m) _Pragma("unroll") for (int k = 0; k < 2; ++k) dst[m][k] = *(const PG8_LAS bf16x8*)(lds + PG8_SA(b, h) + aoff + m * 2048 + k * 1024); } while (0)
; #define PG8_LDB(dst, b, h) do { _Pragma("unroll") for (int n = 0; n < 2; ++n) _Pragma("unroll") for (int k = 0; k < 2; ++k) dst[n][k] = *(const PG8_LAS bf16x8*)(lds + PG8_SB(b, h) + boff + n * 2048 + k * 1024); } while (0)
; #define PG8_WAIT_V(n) asm volatile("s_waitcnt vmcnt(" #n ")" ::: "memory")
; #define PG8_WAIT_L(n) asm volatile("s_waitcnt lgkmcnt(" #n ")" ::: "memory")
; #define PG8_BAR __builtin_amdgcn_s_barrier()
; #define PG8_SCHED __builtin_amdgcn_sched_barrier(0)
; template <class Epi, class Sched, bool ALIGN_EPI>
; __device__ __forceinline__ void gemm_phase(PG8_LAS unsigned char* lds, const Gemm g, const Sched& S, const Epi& E, const int tid) {
;     ...
;         const char* nA = has_next ? (const char*)g.A + (size_t)nxt.pm * tstepA + PG8_ACOL(nxt) : cA; const char* nB = has_next ? (const char*)g.Bt + (size_t)nxt.pn * tstepB : cB;
;         for (int t = 0; t < nt; t += 2) {
;             const bool last = (t == nt - 2);
;             const char* a1 = cA + (size_t)(t + 1) * kstepA;
;             const char* a2 = last ? nA : cA + (size_t)(t + 2) * kstepA; const char* b2 = last ? nB : cB + (size_t)(t + 2) * kstepB;
;             const char* a3 = a2 + kstepA; const char* b3 = b2 + kstepB;
;             if (last && has_next) S.a_ready(nxt);
;             PG8_LDB(B0, 0, 0); PG8_LDB(B1, 0, 1); PG8_SCHED; PG8_LDA(At, 0, 0); PG8_STAGE(PG8_SA(1, 1), a1 + hstepA, voffA);
;             PG8_WAIT_V(8); PG8_WAIT_L(0); PG8_BAR; PG8_MMA(0, 0, At, B0); PG8_MMA(0, 1, At, B1); PG8_BAR; PG8_SCHED;
;     ...
; #pragma unroll
;         for (int a = 0; a < 2; ++a)
; #pragma unroll
;             for (int b = 0; b < 2; ++b)
; #pragma unroll
;                 for (int m = 0; m < 4; ++m)
; #pragma unroll
;                     for (int n = 0; n < 2; ++n) acc[a][b][m][n] = (f32x4){0.f, 0.f, 0.f, 0.f};
.LBB0_1395:
	s_add_u32 s50, s18, s68
	s_addc_u32 s51, s19, s69
	s_add_u32 s52, s20, 0x10000
	v_mov_b32_e32 v0, 0
	s_addc_u32 s53, s21, 0
	s_mov_b64 s[20:21], 0
	v_mov_b32_e32 v1, v0
	v_mov_b32_e32 v2, v0
	v_mov_b32_e32 v3, v0
	v_mov_b32_e32 v4, v0
	v_mov_b32_e32 v5, v0
	v_mov_b32_e32 v6, v0
	v_mov_b32_e32 v7, v0
	v_mov_b32_e32 v16, v0
	v_mov_b32_e32 v17, v0
	v_mov_b32_e32 v18, v0
	v_mov_b32_e32 v19, v0
	v_mov_b32_e32 v20, v0
	v_mov_b32_e32 v21, v0
	v_mov_b32_e32 v22, v0
	v_mov_b32_e32 v23, v0
	v_mov_b32_e32 v32, v0
	v_mov_b32_e32 v33, v0
	v_mov_b32_e32 v34, v0
	v_mov_b32_e32 v35, v0
	v_mov_b32_e32 v36, v0
	v_mov_b32_e32 v37, v0
	v_mov_b32_e32 v38, v0
	v_mov_b32_e32 v39, v0
	v_mov_b32_e32 v48, v0
	v_mov_b32_e32 v49, v0
	v_mov_b32_e32 v50, v0
	v_mov_b32_e32 v51, v0
	v_mov_b32_e32 v52, v0
	v_mov_b32_e32 v53, v0
	v_mov_b32_e32 v54, v0
	v_mov_b32_e32 v55, v0
	v_mov_b32_e32 v8, v0
	v_mov_b32_e32 v9, v0
	v_mov_b32_e32 v10, v0
	v_mov_b32_e32 v11, v0
	v_mov_b32_e32 v12, v0
	v_mov_b32_e32 v13, v0
	v_mov_b32_e32 v14, v0
	v_mov_b32_e32 v15, v0
	v_mov_b32_e32 v24, v0
	v_mov_b32_e32 v25, v0
	v_mov_b32_e32 v26, v0
	v_mov_b32_e32 v27, v0
	v_mov_b32_e32 v28, v0
	v_mov_b32_e32 v29, v0
	v_mov_b32_e32 v30, v0
	v_mov_b32_e32 v31, v0
	v_mov_b32_e32 v40, v0
	v_mov_b32_e32 v41, v0
	v_mov_b32_e32 v42, v0
	v_mov_b32_e32 v43, v0
	v_mov_b32_e32 v44, v0
	v_mov_b32_e32 v45, v0
	v_mov_b32_e32 v46, v0
	v_mov_b32_e32 v47, v0
	v_mov_b32_e32 v56, v0
	v_mov_b32_e32 v57, v0
	v_mov_b32_e32 v58, v0
	v_mov_b32_e32 v59, v0
	v_mov_b32_e32 v60, v0
	v_mov_b32_e32 v61, v0
	v_mov_b32_e32 v62, v0
	v_mov_b32_e32 v63, v0
	v_mov_b32_e32 v64, v0
	v_mov_b32_e32 v65, v0
	v_mov_b32_e32 v66, v0
	v_mov_b32_e32 v67, v0
	v_mov_b32_e32 v68, v0
	v_mov_b32_e32 v69, v0
	v_mov_b32_e32 v70, v0
	v_mov_b32_e32 v71, v0
	v_mov_b32_e32 v80, v0
	v_mov_b32_e32 v81, v0
	v_mov_b32_e32 v82, v0
	v_mov_b32_e32 v83, v0
	v_mov_b32_e32 v84, v0
	v_mov_b32_e32 v85, v0
	v_mov_b32_e32 v86, v0
	v_mov_b32_e32 v87, v0
	v_mov_b32_e32 v112, v0
	v_mov_b32_e32 v113, v0
	v_mov_b32_e32 v114, v0
	v_mov_b32_e32 v115, v0
	v_mov_b32_e32 v116, v0
	v_mov_b32_e32 v117, v0
	v_mov_b32_e32 v118, v0
	v_mov_b32_e32 v119, v0
	v_mov_b32_e32 v130, v0
	v_mov_b32_e32 v131, v0
	v_mov_b32_e32 v132, v0
	v_mov_b32_e32 v133, v0
	v_mov_b32_e32 v134, v0
	v_mov_b32_e32 v135, v0
	v_mov_b32_e32 v136, v0
	v_mov_b32_e32 v137, v0
	v_mov_b32_e32 v72, v0
	v_mov_b32_e32 v73, v0
	v_mov_b32_e32 v74, v0
	v_mov_b32_e32 v75, v0
	v_mov_b32_e32 v76, v0
	v_mov_b32_e32 v77, v0
	v_mov_b32_e32 v78, v0
	v_mov_b32_e32 v79, v0
	v_mov_b32_e32 v96, v0
	v_mov_b32_e32 v97, v0
	v_mov_b32_e32 v98, v0
	v_mov_b32_e32 v99, v0
	v_mov_b32_e32 v104, v0
	v_mov_b32_e32 v105, v0
	v_mov_b32_e32 v106, v0
	v_mov_b32_e32 v107, v0
	v_mov_b32_e32 v120, v0
	v_mov_b32_e32 v121, v0
	v_mov_b32_e32 v122, v0
	v_mov_b32_e32 v123, v0
	v_mov_b32_e32 v124, v0
	v_mov_b32_e32 v125, v0
	v_mov_b32_e32 v126, v0
	v_mov_b32_e32 v127, v0
	v_mov_b32_e32 v138, v0
	v_mov_b32_e32 v139, v0
	v_mov_b32_e32 v140, v0
	v_mov_b32_e32 v141, v0
	v_mov_b32_e32 v142, v0
	v_mov_b32_e32 v143, v0
	v_mov_b32_e32 v144, v0
	v_mov_b32_e32 v145, v0
	v_add_u32_e32 v192, 0x10000, v195
.LBB0_1396:
	s_add_u32 s54, s20, 1
	s_addc_u32 s55, s21, 0
	s_add_u32 s22, s20, 2
	s_addc_u32 s23, s21, 0
	s_lshl_b64 s[24:25], s[22:23], s44
	s_add_u32 s21, s18, s24
	s_addc_u32 s24, s19, s25
	s_cmp_eq_u32 s45, s20
	s_cselect_b32 s26, s8, s21
	s_cselect_b32 s27, s9, s24
	s_cselect_b32 s24, s16, s52
	s_cselect_b32 s25, s17, s53
	s_add_u32 s20, s26, s38
	s_addc_u32 s21, s27, 0
	s_add_i32 s56, 0, 0x10000
	s_add_i32 s57, 0, 0x14000
	ds_read_b128 v[88:91], v192
	ds_read_b128 v[92:95], v192 offset:1024
	ds_read_b128 v[100:103], v192 offset:2048
	ds_read_b128 v[108:111], v192 offset:3072
	ds_read_b128 v[146:149], v192 offset:16384
	ds_read_b128 v[150:153], v192 offset:17408
	ds_read_b128 v[154:157], v192 offset:18432
	ds_read_b128 v[158:161], v192 offset:19456
	s_lshl_b64 s[54:55], s[54:55], s44
	s_add_u32 s54, s50, s54
	s_addc_u32 s55, s51, s55
	s_add_i32 m0, s31, 0xc000
	ds_read_b128 v[162:165], v185
	ds_read_b128 v[166:169], v185 offset:1024
	ds_read_b128 v[172:175], v185 offset:2048
	ds_read_b128 v[188:191], v185 offset:3072
	ds_read_b128 v[196:199], v185 offset:4096
	ds_read_b128 v[200:203], v185 offset:5120
	ds_read_b128 v[204:207], v185 offset:6144
	ds_read_b128 v[208:211], v185 offset:7168
	global_load_lds_dwordx4 v176, s[54:55]
	s_add_i32 m0, s31, 0xe000
	s_nop 0
	global_load_lds_dwordx4 v180, s[54:55]
	s_waitcnt vmcnt(8)
	s_waitcnt lgkmcnt(0)
	s_setprio 1
	s_barrier
; #define PG8_STAGE(bufoff, gbase, voff) do { _Pragma("unroll") for (int _i = 0; _i < 2; ++_i) \
;         __builtin_amdgcn_global_load_lds((const unsigned*)((const char*)(gbase) + (voff)[_i]), (PG8_LAS unsigned*)(lds + (bufoff) + ldsw + _i * 8192), 16, 0, 0); } while (0)
; #define PG8_LDA(dst, b, h) do { _Pragma("unroll") for (int m = 0; m < 4; ++m) _Pragma("unroll") for (int k = 0; k < 2; ++k) dst[m][k] = *(const PG8_LAS bf16x8*)(lds + PG8_SA(b, h) + aoff + m * 2048 + k * 1024); } while (0)
; #define PG8_MMA(ai, bj, At, Bt) do { __builtin_amdgcn_s_setprio(1); _Pragma("unroll") for (int m = 0; m < 4; ++m) _Pragma("unroll") for (int n = 0; n < 2; ++n) _Pragma("unroll") for (int k = 0; k < 2; ++k) \
;         acc[ai][bj][m][n] = __builtin_amdgcn_mfma_f32_16x16x32_bf16(Bt[n][k], At[m][k], acc[ai][bj][m][n], 0, 0, 0); __builtin_amdgcn_s_setprio(0); } while (0)
; #define PG8_WAIT_V(n) asm volatile("s_waitcnt vmcnt(" #n ")" ::: "memory")
; #define PG8_WAIT_L(n) asm volatile("s_waitcnt lgkmcnt(" #n ")" ::: "memory")
; #define PG8_BAR __builtin_amdgcn_s_barrier()
; #define PG8_SCHED __builtin_amdgcn_sched_barrier(0)
; template <class Epi, class Sched, bool ALIGN_EPI>
; __device__ __forceinline__ void gemm_phase(PG8_LAS unsigned char* lds, const Gemm g, const Sched& S, const Epi& E, const int tid) {
;     ...
;             PG8_WAIT_V(8); PG8_WAIT_L(0); PG8_BAR; PG8_MMA(0, 0, At, B0); PG8_MMA(0, 1, At, B1); PG8_BAR; PG8_SCHED;
;             PG8_LDA(At, 0, 1); PG8_STAGE(PG8_SB(0, 0), b2, voffB); PG8_STAGE(PG8_SB(0, 1), b2 + hstepB, voffB); PG8_STAGE(PG8_SA(0, 0), a2, voffA);
;             PG8_WAIT_V(8); PG8_WAIT_L(0); PG8_BAR; PG8_MMA(1, 0, At, B0); PG8_MMA(1, 1, At, B1); PG8_BAR; PG8_SCHED;
	v_mfma_f32_16x16x32_bf16 v[142:145], v[88:91], v[162:165], v[142:145]
	v_mfma_f32_16x16x32_bf16 v[138:141], v[100:103], v[162:165], v[138:141]
	v_mfma_f32_16x16x32_bf16 v[124:127], v[88:91], v[172:175], v[124:127]
	v_mfma_f32_16x16x32_bf16 v[120:123], v[100:103], v[172:175], v[120:123]
	v_mfma_f32_16x16x32_bf16 v[104:107], v[88:91], v[196:199], v[104:107]
	v_mfma_f32_16x16x32_bf16 v[96:99], v[100:103], v[196:199], v[96:99]
	v_mfma_f32_16x16x32_bf16 v[76:79], v[88:91], v[204:207], v[76:79]
	v_mfma_f32_16x16x32_bf16 v[72:75], v[100:103], v[204:207], v[72:75]
	v_mfma_f32_16x16x32_bf16 v[142:145], v[92:95], v[166:169], v[142:145]
	v_mfma_f32_16x16x32_bf16 v[138:141], v[108:111], v[166:169], v[138:141]
	v_mfma_f32_16x16x32_bf16 v[124:127], v[92:95], v[188:191], v[124:127]
	v_mfma_f32_16x16x32_bf16 v[120:123], v[108:111], v[188:191], v[120:123]
	v_mfma_f32_16x16x32_bf16 v[104:107], v[92:95], v[200:203], v[104:107]
	v_mfma_f32_16x16x32_bf16 v[96:99], v[108:111], v[200:203], v[96:99]
	v_mfma_f32_16x16x32_bf16 v[76:79], v[92:95], v[208:211], v[76:79]
	v_mfma_f32_16x16x32_bf16 v[72:75], v[108:111], v[208:211], v[72:75]
	v_mfma_f32_16x16x32_bf16 v[134:137], v[146:149], v[162:165], v[134:137]
	v_mfma_f32_16x16x32_bf16 v[130:133], v[154:157], v[162:165], v[130:133]
	v_mfma_f32_16x16x32_bf16 v[116:119], v[146:149], v[172:175], v[116:119]
	v_mfma_f32_16x16x32_bf16 v[112:115], v[154:157], v[172:175], v[112:115]
	v_mfma_f32_16x16x32_bf16 v[84:87], v[146:149], v[196:199], v[84:87]
	v_mfma_f32_16x16x32_bf16 v[80:83], v[154:157], v[196:199], v[80:83]
	v_mfma_f32_16x16x32_bf16 v[68:71], v[146:149], v[204:207], v[68:71]
	v_mfma_f32_16x16x32_bf16 v[64:67], v[154:157], v[204:207], v[64:67]
	v_mfma_f32_16x16x32_bf16 v[134:137], v[150:153], v[166:169], v[134:137]
	v_mfma_f32_16x16x32_bf16 v[130:133], v[158:161], v[166:169], v[130:133]
	v_mfma_f32_16x16x32_bf16 v[116:119], v[150:153], v[188:191], v[116:119]
	v_mfma_f32_16x16x32_bf16 v[112:115], v[158:161], v[188:191], v[112:115]
	v_mfma_f32_16x16x32_bf16 v[84:87], v[150:153], v[200:203], v[84:87]
	v_mfma_f32_16x16x32_bf16 v[80:83], v[158:161], v[200:203], v[80:83]
	v_mfma_f32_16x16x32_bf16 v[68:71], v[150:153], v[208:211], v[68:71]
	v_mfma_f32_16x16x32_bf16 v[64:67], v[158:161], v[208:211], v[64:67]
	s_barrier
	s_setprio 0
	s_add_i32 s54, s56, s30
	s_mov_b32 m0, s54
	ds_read_b128 v[162:165], v185 offset:16384
	ds_read_b128 v[166:169], v185 offset:17408
	ds_read_b128 v[172:175], v185 offset:18432
	ds_read_b128 v[188:191], v185 offset:19456
	ds_read_b128 v[196:199], v185 offset:20480
	ds_read_b128 v[200:203], v185 offset:21504
	ds_read_b128 v[204:207], v185 offset:22528
	ds_read_b128 v[208:211], v185 offset:23552
	global_load_lds_dwordx4 v178, s[24:25]
	s_add_i32 m0, s54, 0x2000
	s_add_u32 s54, s24, 0x4000
	s_addc_u32 s55, s25, 0
	s_add_i32 s56, s57, s30
	global_load_lds_dwordx4 v182, s[24:25]
	s_mov_b32 m0, s56
	s_nop 0
	global_load_lds_dwordx4 v178, s[54:55]
	s_add_i32 m0, s56, 0x2000
	s_nop 0
	global_load_lds_dwordx4 v182, s[54:55]
	s_mov_b32 m0, s31
	s_nop 0
	global_load_lds_dwordx4 v176, s[26:27]
	s_mov_b32 m0, s33
	s_nop 0
	global_load_lds_dwordx4 v180, s[26:27]
	s_waitcnt vmcnt(8)
	s_waitcnt lgkmcnt(0)
	s_setprio 1
	s_barrier
	v_mfma_f32_16x16x32_bf16 v[60:63], v[88:91], v[162:165], v[60:63]
	v_mfma_f32_16x16x32_bf16 v[56:59], v[100:103], v[162:165], v[56:59]
	v_mfma_f32_16x16x32_bf16 v[44:47], v[88:91], v[172:175], v[44:47]
	v_mfma_f32_16x16x32_bf16 v[40:43], v[100:103], v[172:175], v[40:43]
	v_mfma_f32_16x16x32_bf16 v[28:31], v[88:91], v[196:199], v[28:31]
	v_mfma_f32_16x16x32_bf16 v[24:27], v[100:103], v[196:199], v[24:27]
	v_mfma_f32_16x16x32_bf16 v[12:15], v[88:91], v[204:207], v[12:15]
	v_mfma_f32_16x16x32_bf16 v[8:11], v[100:103], v[204:207], v[8:11]
	v_mfma_f32_16x16x32_bf16 v[60:63], v[92:95], v[166:169], v[60:63]
	v_mfma_f32_16x16x32_bf16 v[56:59], v[108:111], v[166:169], v[56:59]
	v_mfma_f32_16x16x32_bf16 v[44:47], v[92:95], v[188:191], v[44:47]
	v_mfma_f32_16x16x32_bf16 v[40:43], v[108:111], v[188:191], v[40:43]
	v_mfma_f32_16x16x32_bf16 v[28:31], v[92:95], v[200:203], v[28:31]
	v_mfma_f32_16x16x32_bf16 v[24:27], v[108:111], v[200:203], v[24:27]
	v_mfma_f32_16x16x32_bf16 v[12:15], v[92:95], v[208:211], v[12:15]
	v_mfma_f32_16x16x32_bf16 v[8:11], v[108:111], v[208:211], v[8:11]
	v_mfma_f32_16x16x32_bf16 v[52:55], v[146:149], v[162:165], v[52:55]
	v_mfma_f32_16x16x32_bf16 v[48:51], v[154:157], v[162:165], v[48:51]
	v_mfma_f32_16x16x32_bf16 v[36:39], v[146:149], v[172:175], v[36:39]
	v_mfma_f32_16x16x32_bf16 v[32:35], v[154:157], v[172:175], v[32:35]
	v_mfma_f32_16x16x32_bf16 v[20:23], v[146:149], v[196:199], v[20:23]
	v_mfma_f32_16x16x32_bf16 v[16:19], v[154:157], v[196:199], v[16:19]
	v_mfma_f32_16x16x32_bf16 v[4:7], v[146:149], v[204:207], v[4:7]
	v_mfma_f32_16x16x32_bf16 v[0:3], v[154:157], v[204:207], v[0:3]
	v_mfma_f32_16x16x32_bf16 v[52:55], v[150:153], v[166:169], v[52:55]
	v_mfma_f32_16x16x32_bf16 v[48:51], v[158:161], v[166:169], v[48:51]
	v_mfma_f32_16x16x32_bf16 v[36:39], v[150:153], v[188:191], v[36:39]
	v_mfma_f32_16x16x32_bf16 v[32:35], v[158:161], v[188:191], v[32:35]
	v_mfma_f32_16x16x32_bf16 v[20:23], v[150:153], v[200:203], v[20:23]
	v_mfma_f32_16x16x32_bf16 v[16:19], v[158:161], v[200:203], v[16:19]
	v_mfma_f32_16x16x32_bf16 v[4:7], v[150:153], v[208:211], v[4:7]
	v_mfma_f32_16x16x32_bf16 v[0:3], v[158:161], v[208:211], v[0:3]
	s_barrier
; #define PG8_STAGE(bufoff, gbase, voff) do { _Pragma("unroll") for (int _i = 0; _i < 2; ++_i) \
;         __builtin_amdgcn_global_load_lds((const unsigned*)((const char*)(gbase) + (voff)[_i]), (PG8_LAS unsigned*)(lds + (bufoff) + ldsw + _i * 8192), 16, 0, 0); } while (0)
; #define PG8_LDA(dst, b, h) do { _Pragma("unroll") for (int m = 0; m < 4; ++m) _Pragma("unroll") for (int k = 0; k < 2; ++k) dst[m][k] = *(const PG8_LAS bf16x8*)(lds + PG8_SA(b, h) + aoff + m * 2048 + k * 1024); } while (0)
; #define PG8_LDB(dst, b, h) do { _Pragma("unroll") for (int n = 0; n < 2; ++n) _Pragma("unroll") for (int k = 0; k < 2; ++k) dst[n][k] = *(const PG8_LAS bf16x8*)(lds + PG8_SB(b, h) + boff + n * 2048 + k * 1024); } while (0)
; #define PG8_MMA(ai, bj, At, Bt) do { __builtin_amdgcn_s_setprio(1); _Pragma("unroll") for (int m = 0; m < 4; ++m) _Pragma("unroll") for (int n = 0; n < 2; ++n) _Pragma("unroll") for (int k = 0; k < 2; ++k) \
;         acc[ai][bj][m][n] = __builtin_amdgcn_mfma_f32_16x16x32_bf16(Bt[n][k], At[m][k], acc[ai][bj][m][n], 0, 0, 0); __builtin_amdgcn_s_setprio(0); } while (0)
; #define PG8_WAIT_V(n) asm volatile("s_waitcnt vmcnt(" #n ")" ::: "memory")
; #define PG8_WAIT_L(n) asm volatile("s_waitcnt lgkmcnt(" #n ")" ::: "memory")
; #define PG8_BAR __builtin_amdgcn_s_barrier()
; #define PG8_SCHED __builtin_amdgcn_sched_barrier(0)
; template <class Epi, class Sched, bool ALIGN_EPI>
; __device__ __forceinline__ void gemm_phase(PG8_LAS unsigned char* lds, const Gemm g, const Sched& S, const Epi& E, const int tid) {
;     ...
;             PG8_LDB(B0, 1, 0); PG8_LDB(B1, 1, 1); PG8_SCHED; PG8_LDA(At, 1, 0); PG8_STAGE(PG8_SA(0, 1), a2 + hstepA, voffA);
;             PG8_WAIT_V(8); PG8_WAIT_L(0); PG8_BAR; PG8_MMA(0, 0, At, B0); PG8_MMA(0, 1, At, B1); PG8_BAR; PG8_SCHED;
;             PG8_LDA(At, 1, 1); PG8_STAGE(PG8_SB(1, 0), b3, voffB); PG8_STAGE(PG8_SB(1, 1), b3 + hstepB, voffB); PG8_STAGE(PG8_SA(1, 0), a3, voffA);
;             PG8_WAIT_V(8); PG8_WAIT_L(0); PG8_BAR; PG8_MMA(1, 0, At, B0); PG8_MMA(1, 1, At, B1); PG8_BAR; PG8_SCHED;
;         }
	s_setprio 0
	s_add_i32 s54, 0, 0x18000
	s_add_i32 s55, 0, 0x1c000
	ds_read_b128 v[88:91], v192 offset:32768
	ds_read_b128 v[92:95], v192 offset:33792
	ds_read_b128 v[100:103], v192 offset:34816
	ds_read_b128 v[108:111], v192 offset:35840
	ds_read_b128 v[146:149], v192 offset:49152
	ds_read_b128 v[150:153], v192 offset:50176
	ds_read_b128 v[154:157], v192 offset:51200
	ds_read_b128 v[158:161], v192 offset:52224
	s_add_u32 s26, s26, s68
	s_addc_u32 s27, s27, s69
	s_mov_b32 m0, s34
	ds_read_b128 v[162:165], v185 offset:32768
	ds_read_b128 v[166:169], v185 offset:33792
	ds_read_b128 v[172:175], v185 offset:34816
	ds_read_b128 v[188:191], v185 offset:35840
	ds_read_b128 v[196:199], v185 offset:36864
	ds_read_b128 v[200:203], v185 offset:37888
	ds_read_b128 v[204:207], v185 offset:38912
	ds_read_b128 v[208:211], v185 offset:39936
	global_load_lds_dwordx4 v176, s[26:27]
	s_mov_b32 m0, s35
	s_nop 0
	global_load_lds_dwordx4 v180, s[26:27]
	s_waitcnt vmcnt(8)
	s_waitcnt lgkmcnt(0)
	s_setprio 1
	s_barrier
	v_mfma_f32_16x16x32_bf16 v[142:145], v[88:91], v[162:165], v[142:145]
	v_mfma_f32_16x16x32_bf16 v[138:141], v[100:103], v[162:165], v[138:141]
	v_mfma_f32_16x16x32_bf16 v[124:127], v[88:91], v[172:175], v[124:127]
	v_mfma_f32_16x16x32_bf16 v[120:123], v[100:103], v[172:175], v[120:123]
	v_mfma_f32_16x16x32_bf16 v[104:107], v[88:91], v[196:199], v[104:107]
	v_mfma_f32_16x16x32_bf16 v[96:99], v[100:103], v[196:199], v[96:99]
	v_mfma_f32_16x16x32_bf16 v[76:79], v[88:91], v[204:207], v[76:79]
	v_mfma_f32_16x16x32_bf16 v[72:75], v[100:103], v[204:207], v[72:75]
	v_mfma_f32_16x16x32_bf16 v[142:145], v[92:95], v[166:169], v[142:145]
	v_mfma_f32_16x16x32_bf16 v[138:141], v[108:111], v[166:169], v[138:141]
	v_mfma_f32_16x16x32_bf16 v[124:127], v[92:95], v[188:191], v[124:127]
	v_mfma_f32_16x16x32_bf16 v[120:123], v[108:111], v[188:191], v[120:123]
	v_mfma_f32_16x16x32_bf16 v[104:107], v[92:95], v[200:203], v[104:107]
	v_mfma_f32_16x16x32_bf16 v[96:99], v[108:111], v[200:203], v[96:99]
	v_mfma_f32_16x16x32_bf16 v[76:79], v[92:95], v[208:211], v[76:79]
	v_mfma_f32_16x16x32_bf16 v[72:75], v[108:111], v[208:211], v[72:75]
	v_mfma_f32_16x16x32_bf16 v[134:137], v[146:149], v[162:165], v[134:137]
	v_mfma_f32_16x16x32_bf16 v[130:133], v[154:157], v[162:165], v[130:133]
	v_mfma_f32_16x16x32_bf16 v[116:119], v[146:149], v[172:175], v[116:119]
	v_mfma_f32_16x16x32_bf16 v[112:115], v[154:157], v[172:175], v[112:115]
	v_mfma_f32_16x16x32_bf16 v[84:87], v[146:149], v[196:199], v[84:87]
	v_mfma_f32_16x16x32_bf16 v[80:83], v[154:157], v[196:199], v[80:83]
	v_mfma_f32_16x16x32_bf16 v[68:71], v[146:149], v[204:207], v[68:71]
	v_mfma_f32_16x16x32_bf16 v[64:67], v[154:157], v[204:207], v[64:67]
	v_mfma_f32_16x16x32_bf16 v[134:137], v[150:153], v[166:169], v[134:137]
	v_mfma_f32_16x16x32_bf16 v[130:133], v[158:161], v[166:169], v[130:133]
	v_mfma_f32_16x16x32_bf16 v[116:119], v[150:153], v[188:191], v[116:119]
	v_mfma_f32_16x16x32_bf16 v[112:115], v[158:161], v[188:191], v[112:115]
	v_mfma_f32_16x16x32_bf16 v[84:87], v[150:153], v[200:203], v[84:87]
	v_mfma_f32_16x16x32_bf16 v[80:83], v[158:161], v[200:203], v[80:83]
	v_mfma_f32_16x16x32_bf16 v[68:71], v[150:153], v[208:211], v[68:71]
	v_mfma_f32_16x16x32_bf16 v[64:67], v[158:161], v[208:211], v[64:67]
	s_barrier
	s_setprio 0
	s_add_u32 s26, s24, 0x8000
	s_addc_u32 s27, s25, 0
	s_add_i32 s54, s54, s30
	s_mov_b32 m0, s54
	ds_read_b128 v[162:165], v185 offset:49152
	ds_read_b128 v[166:169], v185 offset:50176
	ds_read_b128 v[172:175], v185 offset:51200
	ds_read_b128 v[188:191], v185 offset:52224
	ds_read_b128 v[196:199], v185 offset:53248
	ds_read_b128 v[200:203], v185 offset:54272
	ds_read_b128 v[204:207], v185 offset:55296
	ds_read_b128 v[208:211], v185 offset:56320
	global_load_lds_dwordx4 v178, s[26:27]
	s_add_i32 m0, s54, 0x2000
	s_add_u32 s24, s24, 0xc000
	s_addc_u32 s25, s25, 0
	global_load_lds_dwordx4 v182, s[26:27]
	s_add_i32 s26, s55, s30
	s_mov_b32 m0, s26
	s_nop 0
	global_load_lds_dwordx4 v178, s[24:25]
	s_add_i32 m0, s26, 0x2000
	s_nop 0
	global_load_lds_dwordx4 v182, s[24:25]
	s_mov_b32 m0, s40
	s_nop 0
	global_load_lds_dwordx4 v176, s[20:21]
	s_mov_b32 m0, s41
	s_nop 0
	global_load_lds_dwordx4 v180, s[20:21]
	s_waitcnt vmcnt(8)
	s_waitcnt lgkmcnt(0)
	s_setprio 1
	s_barrier
	v_mfma_f32_16x16x32_bf16 v[60:63], v[88:91], v[162:165], v[60:63]
	v_mfma_f32_16x16x32_bf16 v[56:59], v[100:103], v[162:165], v[56:59]
	v_mfma_f32_16x16x32_bf16 v[44:47], v[88:91], v[172:175], v[44:47]
	v_mfma_f32_16x16x32_bf16 v[40:43], v[100:103], v[172:175], v[40:43]
	v_mfma_f32_16x16x32_bf16 v[28:31], v[88:91], v[196:199], v[28:31]
	v_mfma_f32_16x16x32_bf16 v[24:27], v[100:103], v[196:199], v[24:27]
	v_mfma_f32_16x16x32_bf16 v[12:15], v[88:91], v[204:207], v[12:15]
	v_mfma_f32_16x16x32_bf16 v[8:11], v[100:103], v[204:207], v[8:11]
	v_mfma_f32_16x16x32_bf16 v[60:63], v[92:95], v[166:169], v[60:63]
	v_mfma_f32_16x16x32_bf16 v[56:59], v[108:111], v[166:169], v[56:59]
	v_mfma_f32_16x16x32_bf16 v[44:47], v[92:95], v[188:191], v[44:47]
	v_mfma_f32_16x16x32_bf16 v[40:43], v[108:111], v[188:191], v[40:43]
	v_mfma_f32_16x16x32_bf16 v[28:31], v[92:95], v[200:203], v[28:31]
	v_mfma_f32_16x16x32_bf16 v[24:27], v[108:111], v[200:203], v[24:27]
	v_mfma_f32_16x16x32_bf16 v[12:15], v[92:95], v[208:211], v[12:15]
	v_mfma_f32_16x16x32_bf16 v[8:11], v[108:111], v[208:211], v[8:11]
	v_mfma_f32_16x16x32_bf16 v[52:55], v[146:149], v[162:165], v[52:55]
	v_mfma_f32_16x16x32_bf16 v[48:51], v[154:157], v[162:165], v[48:51]
	v_mfma_f32_16x16x32_bf16 v[36:39], v[146:149], v[172:175], v[36:39]
	v_mfma_f32_16x16x32_bf16 v[32:35], v[154:157], v[172:175], v[32:35]
	v_mfma_f32_16x16x32_bf16 v[20:23], v[146:149], v[196:199], v[20:23]
	v_mfma_f32_16x16x32_bf16 v[16:19], v[154:157], v[196:199], v[16:19]
	v_mfma_f32_16x16x32_bf16 v[4:7], v[146:149], v[204:207], v[4:7]
	v_mfma_f32_16x16x32_bf16 v[0:3], v[154:157], v[204:207], v[0:3]
	v_mfma_f32_16x16x32_bf16 v[52:55], v[150:153], v[166:169], v[52:55]
	v_mfma_f32_16x16x32_bf16 v[48:51], v[158:161], v[166:169], v[48:51]
	v_mfma_f32_16x16x32_bf16 v[36:39], v[150:153], v[188:191], v[36:39]
	v_mfma_f32_16x16x32_bf16 v[32:35], v[158:161], v[188:191], v[32:35]
	v_mfma_f32_16x16x32_bf16 v[20:23], v[150:153], v[200:203], v[20:23]
	v_mfma_f32_16x16x32_bf16 v[16:19], v[158:161], v[200:203], v[16:19]
	v_mfma_f32_16x16x32_bf16 v[4:7], v[150:153], v[208:211], v[4:7]
	v_mfma_f32_16x16x32_bf16 v[0:3], v[158:161], v[208:211], v[0:3]
	s_barrier
	s_setprio 0
	s_add_u32 s52, s52, 0x10000
	s_addc_u32 s53, s53, 0
	s_cmp_ge_u32 s22, s37
	s_mov_b64 s[20:21], s[22:23]
	s_cbranch_scc0 .LBB0_1396
	s_and_b64 vcc, exec, s[14:15]
	s_cbranch_vccz .LBB0_1399
	s_barrier
